# attention loop: s_setprio 1 window starting before the 5th QK MFMA (alternative window start to the after-2nd-MFMA variant)
# baseline (speedup 1.0000x reference)
; template <bool FIRST>
; __device__ __forceinline__ void partialSM(f32x16& p0, f32x16& p1, float& m_reg, f32x16& nm16, float& alpha) {
;     ...
;   for (int r = 0; r < 16; ++r) p0[r] = __builtin_amdgcn_exp2f(p0[r]);
; }
; __device__ __forceinline__ void finishSM(f32x16& p0, f32x16& p1, float alpha, float& l_reg, v8i& pa) {
; #pragma unroll
;   for (int r = 0; r < 16; ++r) p1[r] = __builtin_amdgcn_exp2f(p1[r]);
;   float ps = 0;
; #pragma unroll
;   for (int r = 0; r < 16; ++r) ps += p0[r];
; #pragma unroll
;   for (int r = 0; r < 16; ++r) ps += p1[r];
;   { auto rr = __builtin_amdgcn_permlane32_swap(__float_as_uint(ps), __float_as_uint(ps), false, false);
;     ps = __uint_as_float(rr[0]) + __uint_as_float(rr[1]); }
;   l_reg = l_reg * alpha + ps;
; #pragma unroll
;   for (int q = 0; q < 4; ++q) { int w0 = pa[q], w1 = pa[4 + q];
;     w0 = __builtin_amdgcn_cvt_pk_fp8_f32(p0[4 * q], p0[4 * q + 1], w0, false); w0 = __builtin_amdgcn_cvt_pk_fp8_f32(p0[4 * q + 2], p0[4 * q + 3], w0, true);
;     w1 = __builtin_amdgcn_cvt_pk_fp8_f32(p1[4 * q], p1[4 * q + 1], w1, false); w1 = __builtin_amdgcn_cvt_pk_fp8_f32(p1[4 * q + 2], p1[4 * q + 3], w1, true);
;     pa[q] = w0; pa[4 + q] = w1; }
; }
; __device__ __forceinline__ void qkt(f32x16& p0, f32x16& p1, const char* Ks, const v8i* qr, int r32, int hi, const f32x16& nm16) {
; #pragma unroll
;   for (int s = 0; s < 3; ++s) { const int c0 = 4 * s + 2 * hi;
;     const v8i a0 = __builtin_shufflevector(*reinterpret_cast<const v4i*>(Ks + k8_off(r32, c0)), *reinterpret_cast<const v4i*>(Ks + k8_off(r32, c0 + 1)), 0, 1, 2, 3, 4, 5, 6, 7);
;     const v8i a1 = __builtin_shufflevector(*reinterpret_cast<const v4i*>(Ks + 32 * DQK + k8_off(r32, c0)), *reinterpret_cast<const v4i*>(Ks + 32 * DQK + k8_off(r32, c0 + 1)), 0, 1, 2, 3, 4, 5, 6, 7);
;     p0 = __builtin_amdgcn_mfma_scale_f32_32x32x64_f8f6f4(a0, qr[s], s == 0 ? nm16 : p0, 0, 0, 0, 0, 0, 0);
;     p1 = __builtin_amdgcn_mfma_scale_f32_32x32x64_f8f6f4(a1, qr[s], s == 0 ? nm16 : p1, 0, 0, 0, 0, 0, 0); }
; }
.Lstg_top_l0:
	ds_read_b128 v[98:101], v196 offset:20480
	ds_read_b128 v[102:105], v197 offset:20480
	ds_read_b128 v[206:209], v196 offset:26624
	ds_read_b128 v[210:213], v197 offset:26624
	v_add_f32_e32 v182, 0, v235
	v_add_f32_e32 v182, v236, v182
	s_waitcnt lgkmcnt(0)
	v_mfma_f32_32x32x64_f8f6f4 v[114:129], v[98:105], v[138:145], v[66:81]
	v_add_f32_e32 v182, v233, v182
	v_add_f32_e32 v182, v234, v182
	v_add_f32_e32 v182, v231, v182
	v_add_f32_e32 v182, v232, v182
	v_add_f32_e32 v182, v229, v182
	v_add_f32_e32 v182, v230, v182
	v_add_f32_e32 v182, v227, v182
	v_add_f32_e32 v182, v228, v182
	v_add_f32_e32 v182, v225, v182
	v_add_f32_e32 v182, v226, v182
	v_exp_f32_e32 v82, v82
	v_add_f32_e32 v182, v223, v182
	v_exp_f32_e32 v83, v83
	v_add_f32_e32 v182, v224, v182
	v_exp_f32_e32 v84, v84
	v_mfma_f32_32x32x64_f8f6f4 v[98:113], v[206:213], v[138:145], v[66:81]
	ds_read_b128 v[206:209], v198 offset:20480
	ds_read_b128 v[210:213], v199 offset:20480
	ds_read_b128 v[238:241], v198 offset:26624
	ds_read_b128 v[242:245], v199 offset:26624
	v_add_f32_e32 v182, v221, v182
	v_exp_f32_e32 v85, v85
	v_add_f32_e32 v182, v222, v182
	v_exp_f32_e32 v86, v86
	v_add_f32_e32 v182, v82, v182
	v_exp_f32_e32 v87, v87
	v_add_f32_e32 v182, v83, v182
	v_exp_f32_e32 v88, v88
	v_add_f32_e32 v182, v84, v182
	v_exp_f32_e32 v89, v89
	v_add_f32_e32 v182, v85, v182
	v_exp_f32_e32 v90, v90
	v_add_f32_e32 v182, v86, v182
	v_exp_f32_e32 v91, v91
	s_waitcnt lgkmcnt(0)
	v_mfma_f32_32x32x64_f8f6f4 v[114:129], v[206:213], v[146:153], v[114:129]
	v_add_f32_e32 v182, v87, v182
	v_exp_f32_e32 v92, v92
	v_exp_f32_e32 v94, v94
	v_exp_f32_e32 v95, v95
	v_add_f32_e32 v182, v88, v182
	v_exp_f32_e32 v93, v93
	v_add_f32_e32 v182, v89, v182
	v_add_f32_e32 v182, v90, v182
	v_add_f32_e32 v182, v91, v182
	v_exp_f32_e32 v96, v96
	v_exp_f32_e32 v97, v97
	v_add_f32_e32 v182, v92, v182
	v_cvt_pk_fp8_f32 v130, v235, v236
	v_cvt_pk_fp8_f32 v134, v82, v83
	v_cvt_pk_fp8_f32 v131, v231, v232
	v_mfma_f32_32x32x64_f8f6f4 v[98:113], v[238:245], v[146:153], v[98:113]
	ds_read_b128 v[206:209], v200 offset:20480
	ds_read_b128 v[210:213], v201 offset:20480
	ds_read_b128 v[238:241], v200 offset:26624
	ds_read_b128 v[242:245], v201 offset:26624
	s_setprio 1
	v_cvt_pk_fp8_f32 v135, v86, v87
	v_cvt_pk_fp8_f32 v132, v227, v228
	v_cvt_pk_fp8_f32 v136, v90, v91
	v_cvt_pk_fp8_f32 v133, v223, v224
	v_cvt_pk_fp8_f32 v137, v94, v95
	v_add_f32_e32 v182, v93, v182
	v_add_f32_e32 v182, v94, v182
	v_add_f32_e32 v182, v95, v182
	v_add_f32_e32 v182, v96, v182
	v_cvt_pk_fp8_f32 v130, v233, v234 op_sel:[0,0,1]
	v_cvt_pk_fp8_f32 v134, v84, v85 op_sel:[0,0,1]
	v_cvt_pk_fp8_f32 v131, v229, v230 op_sel:[0,0,1]
	v_cvt_pk_fp8_f32 v135, v88, v89 op_sel:[0,0,1]
	v_cvt_pk_fp8_f32 v132, v225, v226 op_sel:[0,0,1]
	s_waitcnt lgkmcnt(0)
	v_mfma_f32_32x32x64_f8f6f4 v[114:129], v[206:213], v[154:161], v[114:129]
	v_cvt_pk_fp8_f32 v136, v92, v93 op_sel:[0,0,1]
	v_cvt_pk_fp8_f32 v133, v221, v222 op_sel:[0,0,1]
	v_cvt_pk_fp8_f32 v137, v96, v97 op_sel:[0,0,1]
	v_add_f32_e32 v206, v97, v182
	v_mov_b32_e32 v207, v206
	s_nop 1
	v_permlane32_swap_b32_e32 v206, v207
	v_mfma_f32_32x32x64_f8f6f4 v[98:113], v[238:245], v[154:161], v[98:113]
	s_cmp_eq_u32 s94, 0
	s_cbranch_scc0 .Lstg_mid0_l0
	s_waitcnt vmcnt(0)
	s_barrier
	s_mov_b32 m0, s87
	s_nop 0
	global_load_lds_dwordx4 v164, s[24:25]
	s_mov_b32 m0, s89
	s_nop 0
	global_load_lds_dwordx4 v170, s[26:27]
	s_add_u32 s24, s24, 0x3000
	s_addc_u32 s25, s25, 0
	s_add_u32 s26, s26, 64
	s_addc_u32 s27, s27, 0

; template <bool FIRST>
; __device__ __forceinline__ void partialSM(f32x16& p0, f32x16& p1, float& m_reg, f32x16& nm16, float& alpha) {
;     ...
;   for (int r = 0; r < 16; ++r) p0[r] = __builtin_amdgcn_exp2f(p0[r]);
; }
; __device__ __forceinline__ void finishSM(f32x16& p0, f32x16& p1, float alpha, float& l_reg, v8i& pa) {
; #pragma unroll
;   for (int r = 0; r < 16; ++r) p1[r] = __builtin_amdgcn_exp2f(p1[r]);
;   float ps = 0;
; #pragma unroll
;   for (int r = 0; r < 16; ++r) ps += p0[r];
; #pragma unroll
;   for (int r = 0; r < 16; ++r) ps += p1[r];
;   { auto rr = __builtin_amdgcn_permlane32_swap(__float_as_uint(ps), __float_as_uint(ps), false, false);
;     ps = __uint_as_float(rr[0]) + __uint_as_float(rr[1]); }
;   l_reg = l_reg * alpha + ps;
; #pragma unroll
;   for (int q = 0; q < 4; ++q) { int w0 = pa[q], w1 = pa[4 + q];
;     w0 = __builtin_amdgcn_cvt_pk_fp8_f32(p0[4 * q], p0[4 * q + 1], w0, false); w0 = __builtin_amdgcn_cvt_pk_fp8_f32(p0[4 * q + 2], p0[4 * q + 3], w0, true);
;     w1 = __builtin_amdgcn_cvt_pk_fp8_f32(p1[4 * q], p1[4 * q + 1], w1, false); w1 = __builtin_amdgcn_cvt_pk_fp8_f32(p1[4 * q + 2], p1[4 * q + 3], w1, true);
;     pa[q] = w0; pa[4 + q] = w1; }
; }
; __device__ __forceinline__ void qkt(f32x16& p0, f32x16& p1, const char* Ks, const v8i* qr, int r32, int hi, const f32x16& nm16) {
; #pragma unroll
;   for (int s = 0; s < 3; ++s) { const int c0 = 4 * s + 2 * hi;
;     const v8i a0 = __builtin_shufflevector(*reinterpret_cast<const v4i*>(Ks + k8_off(r32, c0)), *reinterpret_cast<const v4i*>(Ks + k8_off(r32, c0 + 1)), 0, 1, 2, 3, 4, 5, 6, 7);
;     const v8i a1 = __builtin_shufflevector(*reinterpret_cast<const v4i*>(Ks + 32 * DQK + k8_off(r32, c0)), *reinterpret_cast<const v4i*>(Ks + 32 * DQK + k8_off(r32, c0 + 1)), 0, 1, 2, 3, 4, 5, 6, 7);
;     p0 = __builtin_amdgcn_mfma_scale_f32_32x32x64_f8f6f4(a0, qr[s], s == 0 ? nm16 : p0, 0, 0, 0, 0, 0, 0);
;     p1 = __builtin_amdgcn_mfma_scale_f32_32x32x64_f8f6f4(a1, qr[s], s == 0 ? nm16 : p1, 0, 0, 0, 0, 0, 0); }
; }
.Lstg_end0_l0:
	v_exp_f32_e32 v182, v114
	v_exp_f32_e32 v183, v115
	v_exp_f32_e32 v184, v116
	v_exp_f32_e32 v185, v117
	v_exp_f32_e32 v226, v118
	v_exp_f32_e32 v227, v119
	v_exp_f32_e32 v228, v120
	v_exp_f32_e32 v229, v121
	v_exp_f32_e32 v230, v122
	v_exp_f32_e32 v231, v123
	v_exp_f32_e32 v232, v124
	v_exp_f32_e32 v233, v125
	v_exp_f32_e32 v234, v126
	v_exp_f32_e32 v235, v127
	v_exp_f32_e32 v236, v128
	v_exp_f32_e32 v237, v129
	ds_read_b128 v[82:85], v196 offset:49152
	ds_read_b128 v[86:89], v197 offset:49152
	ds_read_b128 v[210:213], v196 offset:55296
	ds_read_b128 v[214:217], v197 offset:55296
	v_add_f32_e32 v209, 0, v182
	v_add_f32_e32 v209, v183, v209
	s_waitcnt lgkmcnt(0)
	v_mfma_f32_32x32x64_f8f6f4 v[114:129], v[82:89], v[138:145], v[66:81]
	v_add_f32_e32 v209, v184, v209
	v_add_f32_e32 v209, v185, v209
	v_add_f32_e32 v209, v226, v209
	v_add_f32_e32 v209, v227, v209
	v_add_f32_e32 v209, v228, v209
	v_add_f32_e32 v209, v229, v209
	v_add_f32_e32 v209, v230, v209
	v_add_f32_e32 v209, v231, v209
	v_add_f32_e32 v209, v232, v209
	v_add_f32_e32 v209, v233, v209
	v_exp_f32_e32 v98, v98
	v_add_f32_e32 v209, v234, v209
	v_exp_f32_e32 v99, v99
	v_add_f32_e32 v209, v235, v209
	v_exp_f32_e32 v100, v100
	v_mfma_f32_32x32x64_f8f6f4 v[82:97], v[210:217], v[138:145], v[66:81]
	ds_read_b128 v[210:213], v198 offset:49152
	ds_read_b128 v[214:217], v199 offset:49152
	ds_read_b128 v[218:221], v198 offset:55296
	ds_read_b128 v[222:225], v199 offset:55296
	v_add_f32_e32 v209, v236, v209
	v_exp_f32_e32 v101, v101
	v_add_f32_e32 v209, v237, v209
	v_exp_f32_e32 v102, v102
	v_add_f32_e32 v209, v98, v209
	v_exp_f32_e32 v103, v103
	v_add_f32_e32 v209, v99, v209
	v_exp_f32_e32 v104, v104
	v_add_f32_e32 v209, v100, v209
	v_exp_f32_e32 v105, v105
	v_add_f32_e32 v209, v101, v209
	v_exp_f32_e32 v106, v106
	v_add_f32_e32 v209, v102, v209
	v_exp_f32_e32 v107, v107
	s_waitcnt lgkmcnt(0)
	v_mfma_f32_32x32x64_f8f6f4 v[114:129], v[210:217], v[146:153], v[114:129]
	v_add_f32_e32 v209, v103, v209
	v_exp_f32_e32 v108, v108
	v_exp_f32_e32 v110, v110
	v_exp_f32_e32 v111, v111
	v_add_f32_e32 v209, v104, v209
	v_exp_f32_e32 v109, v109
	v_add_f32_e32 v209, v105, v209
	v_add_f32_e32 v209, v106, v209
	v_add_f32_e32 v209, v107, v209
	v_exp_f32_e32 v112, v112
	v_exp_f32_e32 v113, v113
	v_add_f32_e32 v209, v108, v209
	v_cvt_pk_fp8_f32 v130, v182, v183
	v_cvt_pk_fp8_f32 v134, v98, v99
	v_cvt_pk_fp8_f32 v131, v226, v227
	v_mfma_f32_32x32x64_f8f6f4 v[82:97], v[218:225], v[146:153], v[82:97]
	ds_read_b128 v[210:213], v200 offset:49152
	ds_read_b128 v[214:217], v201 offset:49152
	ds_read_b128 v[218:221], v200 offset:55296
	ds_read_b128 v[222:225], v201 offset:55296
	s_setprio 1
	v_cvt_pk_fp8_f32 v135, v102, v103
	v_cvt_pk_fp8_f32 v132, v230, v231
	v_cvt_pk_fp8_f32 v136, v106, v107
	v_cvt_pk_fp8_f32 v133, v234, v235
	v_cvt_pk_fp8_f32 v137, v110, v111
	v_add_f32_e32 v209, v109, v209
	v_add_f32_e32 v209, v110, v209
	v_add_f32_e32 v209, v111, v209
	v_add_f32_e32 v209, v112, v209
	v_cvt_pk_fp8_f32 v130, v184, v185 op_sel:[0,0,1]
	v_cvt_pk_fp8_f32 v134, v100, v101 op_sel:[0,0,1]
	v_cvt_pk_fp8_f32 v131, v228, v229 op_sel:[0,0,1]
	v_cvt_pk_fp8_f32 v135, v104, v105 op_sel:[0,0,1]
	v_cvt_pk_fp8_f32 v132, v232, v233 op_sel:[0,0,1]
	s_waitcnt lgkmcnt(0)
	v_mfma_f32_32x32x64_f8f6f4 v[114:129], v[210:217], v[154:161], v[114:129]
	v_cvt_pk_fp8_f32 v136, v108, v109 op_sel:[0,0,1]
	v_cvt_pk_fp8_f32 v133, v236, v237 op_sel:[0,0,1]
	v_cvt_pk_fp8_f32 v137, v112, v113 op_sel:[0,0,1]
	v_add_f32_e32 v209, v113, v209
	v_mov_b32_e32 v210, v209
	s_nop 1
	v_permlane32_swap_b32_e32 v209, v210
	v_mfma_f32_32x32x64_f8f6f4 v[82:97], v[218:225], v[154:161], v[82:97]
	s_cmp_eq_u32 s94, 0
	s_cbranch_scc0 .Lstg_mid1_l0
	s_waitcnt vmcnt(0)
	s_barrier
	s_mov_b32 m0, s92
	s_nop 0
	global_load_lds_dwordx4 v164, s[24:25]
	s_mov_b32 m0, s86
	s_nop 0
	global_load_lds_dwordx4 v170, s[26:27]
	s_add_u32 s24, s24, 0x3000
	s_addc_u32 s25, s25, 0
	s_add_u32 s26, s26, 64
	s_addc_u32 s27, s27, 0

; template <bool FIRST>
; __device__ __forceinline__ void partialSM(f32x16& p0, f32x16& p1, float& m_reg, f32x16& nm16, float& alpha) {
;     ...
;   for (int r = 0; r < 16; ++r) p0[r] = __builtin_amdgcn_exp2f(p0[r]);
; }
; __device__ __forceinline__ void finishSM(f32x16& p0, f32x16& p1, float alpha, float& l_reg, v8i& pa) {
; #pragma unroll
;   for (int r = 0; r < 16; ++r) p1[r] = __builtin_amdgcn_exp2f(p1[r]);
;   float ps = 0;
; #pragma unroll
;   for (int r = 0; r < 16; ++r) ps += p0[r];
; #pragma unroll
;   for (int r = 0; r < 16; ++r) ps += p1[r];
;   { auto rr = __builtin_amdgcn_permlane32_swap(__float_as_uint(ps), __float_as_uint(ps), false, false);
;     ps = __uint_as_float(rr[0]) + __uint_as_float(rr[1]); }
;   l_reg = l_reg * alpha + ps;
; #pragma unroll
;   for (int q = 0; q < 4; ++q) { int w0 = pa[q], w1 = pa[4 + q];
;     w0 = __builtin_amdgcn_cvt_pk_fp8_f32(p0[4 * q], p0[4 * q + 1], w0, false); w0 = __builtin_amdgcn_cvt_pk_fp8_f32(p0[4 * q + 2], p0[4 * q + 3], w0, true);
;     w1 = __builtin_amdgcn_cvt_pk_fp8_f32(p1[4 * q], p1[4 * q + 1], w1, false); w1 = __builtin_amdgcn_cvt_pk_fp8_f32(p1[4 * q + 2], p1[4 * q + 3], w1, true);
;     pa[q] = w0; pa[4 + q] = w1; }
; }
; __device__ __forceinline__ void qkt(f32x16& p0, f32x16& p1, const char* Ks, const v8i* qr, int r32, int hi, const f32x16& nm16) {
; #pragma unroll
;   for (int s = 0; s < 3; ++s) { const int c0 = 4 * s + 2 * hi;
;     const v8i a0 = __builtin_shufflevector(*reinterpret_cast<const v4i*>(Ks + k8_off(r32, c0)), *reinterpret_cast<const v4i*>(Ks + k8_off(r32, c0 + 1)), 0, 1, 2, 3, 4, 5, 6, 7);
;     const v8i a1 = __builtin_shufflevector(*reinterpret_cast<const v4i*>(Ks + 32 * DQK + k8_off(r32, c0)), *reinterpret_cast<const v4i*>(Ks + 32 * DQK + k8_off(r32, c0 + 1)), 0, 1, 2, 3, 4, 5, 6, 7);
;     p0 = __builtin_amdgcn_mfma_scale_f32_32x32x64_f8f6f4(a0, qr[s], s == 0 ? nm16 : p0, 0, 0, 0, 0, 0, 0);
;     p1 = __builtin_amdgcn_mfma_scale_f32_32x32x64_f8f6f4(a1, qr[s], s == 0 ? nm16 : p1, 0, 0, 0, 0, 0, 0); }
; }
.Lstg_end1_l0:
	v_exp_f32_e32 v182, v114
	v_exp_f32_e32 v183, v115
	v_exp_f32_e32 v184, v116
	v_exp_f32_e32 v185, v117
	v_exp_f32_e32 v228, v118
	v_exp_f32_e32 v229, v119
	v_exp_f32_e32 v230, v120
	v_exp_f32_e32 v231, v121
	v_exp_f32_e32 v232, v122
	v_exp_f32_e32 v233, v123
	v_exp_f32_e32 v234, v124
	v_exp_f32_e32 v235, v125
	v_exp_f32_e32 v236, v126
	v_exp_f32_e32 v237, v127
	v_exp_f32_e32 v238, v128
	v_exp_f32_e32 v239, v129
	ds_read_b128 v[98:101], v196 offset:8192
	ds_read_b128 v[102:105], v197 offset:8192
	ds_read_b128 v[212:215], v196 offset:14336
	ds_read_b128 v[216:219], v197 offset:14336
	v_exp_f32_e32 v82, v82
	v_exp_f32_e32 v83, v83
	s_waitcnt lgkmcnt(0)
	v_mfma_f32_32x32x64_f8f6f4 v[114:129], v[98:105], v[138:145], v[66:81]
	v_exp_f32_e32 v84, v84
	v_exp_f32_e32 v85, v85
	v_exp_f32_e32 v86, v86
	v_exp_f32_e32 v87, v87
	v_exp_f32_e32 v88, v88
	v_exp_f32_e32 v89, v89
	v_exp_f32_e32 v90, v90
	v_exp_f32_e32 v91, v91
	v_exp_f32_e32 v92, v92
	v_exp_f32_e32 v94, v94
	v_exp_f32_e32 v95, v95
	v_exp_f32_e32 v93, v93
	v_exp_f32_e32 v96, v96
	v_exp_f32_e32 v97, v97
	v_cvt_pk_fp8_f32 v130, v182, v183
	v_mfma_f32_32x32x64_f8f6f4 v[98:113], v[212:219], v[138:145], v[66:81]
	ds_read_b128 v[212:215], v198 offset:8192
	ds_read_b128 v[216:219], v199 offset:8192
	ds_read_b128 v[220:223], v198 offset:14336
	ds_read_b128 v[224:227], v199 offset:14336
	v_cvt_pk_fp8_f32 v134, v82, v83
	v_cvt_pk_fp8_f32 v131, v228, v229
	v_cvt_pk_fp8_f32 v135, v86, v87
	v_cvt_pk_fp8_f32 v132, v232, v233
	v_cvt_pk_fp8_f32 v136, v90, v91
	v_cvt_pk_fp8_f32 v133, v236, v237
	v_cvt_pk_fp8_f32 v137, v94, v95
	v_cvt_pk_fp8_f32 v130, v184, v185 op_sel:[0,0,1]
	v_cvt_pk_fp8_f32 v134, v84, v85 op_sel:[0,0,1]
	v_cvt_pk_fp8_f32 v131, v230, v231 op_sel:[0,0,1]
	v_cvt_pk_fp8_f32 v135, v88, v89 op_sel:[0,0,1]
	v_cvt_pk_fp8_f32 v132, v234, v235 op_sel:[0,0,1]
	v_cvt_pk_fp8_f32 v136, v92, v93 op_sel:[0,0,1]
	v_cvt_pk_fp8_f32 v133, v238, v239 op_sel:[0,0,1]
	s_waitcnt lgkmcnt(0)
	v_mfma_f32_32x32x64_f8f6f4 v[114:129], v[212:219], v[146:153], v[114:129]
	v_cvt_pk_fp8_f32 v137, v96, v97 op_sel:[0,0,1]
	v_mfma_f32_32x32x64_f8f6f4 v[98:113], v[220:227], v[146:153], v[98:113]
	ds_read_b128 v[212:215], v200 offset:8192
	ds_read_b128 v[216:219], v201 offset:8192
	ds_read_b128 v[220:223], v200 offset:14336
	ds_read_b128 v[224:227], v201 offset:14336
	s_setprio 1
	s_waitcnt lgkmcnt(0)
	v_mfma_f32_32x32x64_f8f6f4 v[114:129], v[212:219], v[154:161], v[114:129]
	v_add_f32_e32 v212, 0, v182
	v_add_f32_e32 v212, v183, v212
	v_add_f32_e32 v212, v184, v212
	v_add_f32_e32 v212, v185, v212
	v_add_f32_e32 v212, v228, v212
	v_add_f32_e32 v212, v229, v212
	v_add_f32_e32 v212, v230, v212
	v_add_f32_e32 v212, v231, v212
	v_add_f32_e32 v212, v232, v212
	v_add_f32_e32 v212, v233, v212
	v_add_f32_e32 v212, v234, v212
	v_add_f32_e32 v212, v235, v212
	v_add_f32_e32 v212, v236, v212
	v_add_f32_e32 v212, v237, v212
	v_add_f32_e32 v212, v238, v212
	v_add_f32_e32 v212, v239, v212
	v_add_f32_e32 v212, v82, v212
	v_add_f32_e32 v212, v83, v212
	v_mfma_f32_32x32x64_f8f6f4 v[98:113], v[220:227], v[154:161], v[98:113]
	v_add_f32_e32 v212, v84, v212
	v_add_f32_e32 v212, v85, v212
	v_add_f32_e32 v212, v86, v212
	v_add_f32_e32 v212, v87, v212
	v_add_f32_e32 v212, v88, v212
	v_add_f32_e32 v212, v89, v212
	v_add_f32_e32 v212, v90, v212
	v_add_f32_e32 v212, v91, v212
	v_add_f32_e32 v212, v92, v212
	v_add_f32_e32 v212, v93, v212
	v_add_f32_e32 v212, v94, v212
	v_add_f32_e32 v212, v95, v212
	v_add_f32_e32 v212, v96, v212
	v_add_f32_e32 v212, v97, v212
	v_mov_b32_e32 v213, v212
	s_nop 1
	v_permlane32_swap_b32_e32 v212, v213
	s_cmp_eq_u32 s94, 0
	s_cbranch_scc0 .Lstg_mid2_l0
	s_waitcnt vmcnt(0)
	s_barrier
	s_mov_b32 m0, s90
	s_nop 0
	global_load_lds_dwordx4 v164, s[24:25]
	s_mov_b32 m0, s88
	s_nop 0
	global_load_lds_dwordx4 v170, s[26:27]
	s_add_u32 s24, s24, 0x3000
	s_addc_u32 s25, s25, 0
	s_add_u32 s26, s26, 64
	s_addc_u32 s27, s27, 0

; template <bool FIRST>
; __device__ __forceinline__ void partialSM(f32x16& p0, f32x16& p1, float& m_reg, f32x16& nm16, float& alpha) {
;     ...
;   for (int r = 0; r < 16; ++r) p0[r] = __builtin_amdgcn_exp2f(p0[r]);
; }
; __device__ __forceinline__ void finishSM(f32x16& p0, f32x16& p1, float alpha, float& l_reg, v8i& pa) {
; #pragma unroll
;   for (int r = 0; r < 16; ++r) p1[r] = __builtin_amdgcn_exp2f(p1[r]);
;   float ps = 0;
; #pragma unroll
;   for (int r = 0; r < 16; ++r) ps += p0[r];
; #pragma unroll
;   for (int r = 0; r < 16; ++r) ps += p1[r];
;   { auto rr = __builtin_amdgcn_permlane32_swap(__float_as_uint(ps), __float_as_uint(ps), false, false);
;     ps = __uint_as_float(rr[0]) + __uint_as_float(rr[1]); }
;   l_reg = l_reg * alpha + ps;
; #pragma unroll
;   for (int q = 0; q < 4; ++q) { int w0 = pa[q], w1 = pa[4 + q];
;     w0 = __builtin_amdgcn_cvt_pk_fp8_f32(p0[4 * q], p0[4 * q + 1], w0, false); w0 = __builtin_amdgcn_cvt_pk_fp8_f32(p0[4 * q + 2], p0[4 * q + 3], w0, true);
;     w1 = __builtin_amdgcn_cvt_pk_fp8_f32(p1[4 * q], p1[4 * q + 1], w1, false); w1 = __builtin_amdgcn_cvt_pk_fp8_f32(p1[4 * q + 2], p1[4 * q + 3], w1, true);
;     pa[q] = w0; pa[4 + q] = w1; }
; }
; __device__ __forceinline__ void qkt(f32x16& p0, f32x16& p1, const char* Ks, const v8i* qr, int r32, int hi, const f32x16& nm16) {
; #pragma unroll
;   for (int s = 0; s < 3; ++s) { const int c0 = 4 * s + 2 * hi;
;     const v8i a0 = __builtin_shufflevector(*reinterpret_cast<const v4i*>(Ks + k8_off(r32, c0)), *reinterpret_cast<const v4i*>(Ks + k8_off(r32, c0 + 1)), 0, 1, 2, 3, 4, 5, 6, 7);
;     const v8i a1 = __builtin_shufflevector(*reinterpret_cast<const v4i*>(Ks + 32 * DQK + k8_off(r32, c0)), *reinterpret_cast<const v4i*>(Ks + 32 * DQK + k8_off(r32, c0 + 1)), 0, 1, 2, 3, 4, 5, 6, 7);
;     p0 = __builtin_amdgcn_mfma_scale_f32_32x32x64_f8f6f4(a0, qr[s], s == 0 ? nm16 : p0, 0, 0, 0, 0, 0, 0);
;     p1 = __builtin_amdgcn_mfma_scale_f32_32x32x64_f8f6f4(a1, qr[s], s == 0 ? nm16 : p1, 0, 0, 0, 0, 0, 0); }
; }
.Lstg_end2_l0:
	v_exp_f32_e32 v182, v114
	v_exp_f32_e32 v183, v115
	v_exp_f32_e32 v184, v116
	v_exp_f32_e32 v185, v117
	v_exp_f32_e32 v232, v118
	v_exp_f32_e32 v233, v119
	v_exp_f32_e32 v234, v120
	v_exp_f32_e32 v235, v121
	v_exp_f32_e32 v236, v122
	v_exp_f32_e32 v237, v123
	v_exp_f32_e32 v238, v124
	v_exp_f32_e32 v239, v125
	v_exp_f32_e32 v240, v126
	v_exp_f32_e32 v241, v127
	v_exp_f32_e32 v242, v128
	v_exp_f32_e32 v243, v129
	ds_read_b128 v[82:85], v196 offset:20480
	ds_read_b128 v[86:89], v197 offset:20480
	ds_read_b128 v[216:219], v196 offset:26624
	ds_read_b128 v[220:223], v197 offset:26624
	v_add_f32_e32 v215, 0, v182
	v_add_f32_e32 v215, v183, v215
	s_waitcnt lgkmcnt(0)
	v_mfma_f32_32x32x64_f8f6f4 v[114:129], v[82:89], v[138:145], v[66:81]
	v_add_f32_e32 v215, v184, v215
	v_add_f32_e32 v215, v185, v215
	v_add_f32_e32 v215, v232, v215
	v_add_f32_e32 v215, v233, v215
	v_add_f32_e32 v215, v234, v215
	v_add_f32_e32 v215, v235, v215
	v_add_f32_e32 v215, v236, v215
	v_add_f32_e32 v215, v237, v215
	v_add_f32_e32 v215, v238, v215
	v_add_f32_e32 v215, v239, v215
	v_exp_f32_e32 v98, v98
	v_add_f32_e32 v215, v240, v215
	v_exp_f32_e32 v99, v99
	v_add_f32_e32 v215, v241, v215
	v_exp_f32_e32 v100, v100
	v_mfma_f32_32x32x64_f8f6f4 v[82:97], v[216:223], v[138:145], v[66:81]
	ds_read_b128 v[216:219], v198 offset:20480
	ds_read_b128 v[220:223], v199 offset:20480
	ds_read_b128 v[224:227], v198 offset:26624
	ds_read_b128 v[228:231], v199 offset:26624
	v_add_f32_e32 v215, v242, v215
	v_exp_f32_e32 v101, v101
	v_add_f32_e32 v215, v243, v215
	v_exp_f32_e32 v102, v102
	v_add_f32_e32 v215, v98, v215
	v_exp_f32_e32 v103, v103
	v_add_f32_e32 v215, v99, v215
	v_exp_f32_e32 v104, v104
	v_add_f32_e32 v215, v100, v215
	v_exp_f32_e32 v105, v105
	v_add_f32_e32 v215, v101, v215
	v_exp_f32_e32 v106, v106
	v_add_f32_e32 v215, v102, v215
	v_exp_f32_e32 v107, v107
	s_waitcnt lgkmcnt(0)
	v_mfma_f32_32x32x64_f8f6f4 v[114:129], v[216:223], v[146:153], v[114:129]
	v_add_f32_e32 v215, v103, v215
	v_exp_f32_e32 v108, v108
	v_exp_f32_e32 v110, v110
	v_exp_f32_e32 v111, v111
	v_add_f32_e32 v215, v104, v215
	v_exp_f32_e32 v109, v109
	v_add_f32_e32 v215, v105, v215
	v_add_f32_e32 v215, v106, v215
	v_add_f32_e32 v215, v107, v215
	v_exp_f32_e32 v112, v112
	v_exp_f32_e32 v113, v113
	v_add_f32_e32 v215, v108, v215
	v_cvt_pk_fp8_f32 v130, v182, v183
	v_cvt_pk_fp8_f32 v134, v98, v99
	v_cvt_pk_fp8_f32 v131, v232, v233
	v_mfma_f32_32x32x64_f8f6f4 v[82:97], v[224:231], v[146:153], v[82:97]
	ds_read_b128 v[216:219], v200 offset:20480
	ds_read_b128 v[220:223], v201 offset:20480
	ds_read_b128 v[224:227], v200 offset:26624
	ds_read_b128 v[228:231], v201 offset:26624
	s_setprio 1
	v_cvt_pk_fp8_f32 v135, v102, v103
	v_cvt_pk_fp8_f32 v132, v236, v237
	v_cvt_pk_fp8_f32 v136, v106, v107
	v_cvt_pk_fp8_f32 v133, v240, v241
	v_cvt_pk_fp8_f32 v137, v110, v111
	v_add_f32_e32 v215, v109, v215
	v_add_f32_e32 v215, v110, v215
	v_add_f32_e32 v215, v111, v215
	v_add_f32_e32 v215, v112, v215
	v_cvt_pk_fp8_f32 v130, v184, v185 op_sel:[0,0,1]
	v_cvt_pk_fp8_f32 v134, v100, v101 op_sel:[0,0,1]
	v_cvt_pk_fp8_f32 v131, v234, v235 op_sel:[0,0,1]
	v_cvt_pk_fp8_f32 v135, v104, v105 op_sel:[0,0,1]
	v_cvt_pk_fp8_f32 v132, v238, v239 op_sel:[0,0,1]
	s_waitcnt lgkmcnt(0)
	v_mfma_f32_32x32x64_f8f6f4 v[114:129], v[216:223], v[154:161], v[114:129]
	v_cvt_pk_fp8_f32 v136, v108, v109 op_sel:[0,0,1]
	v_cvt_pk_fp8_f32 v133, v242, v243 op_sel:[0,0,1]
	v_cvt_pk_fp8_f32 v137, v112, v113 op_sel:[0,0,1]
	v_add_f32_e32 v215, v113, v215
	v_mov_b32_e32 v216, v215
	s_nop 1
	v_permlane32_swap_b32_e32 v215, v216
	v_mfma_f32_32x32x64_f8f6f4 v[82:97], v[224:231], v[154:161], v[82:97]
	s_cmp_eq_u32 s94, 0
	s_cbranch_scc0 .Lstg_mid3_l0
	s_waitcnt vmcnt(0)
	s_barrier
	s_mov_b32 m0, s87
	s_nop 0
	global_load_lds_dwordx4 v164, s[24:25]
	s_mov_b32 m0, s89
	s_nop 0
	global_load_lds_dwordx4 v170, s[26:27]
	s_add_u32 s24, s24, 0x3000
	s_addc_u32 s25, s25, 0
	s_add_u32 s26, s26, 64
	s_addc_u32 s27, s27, 0

; template <bool FIRST>
; __device__ __forceinline__ void partialSM(f32x16& p0, f32x16& p1, float& m_reg, f32x16& nm16, float& alpha) {
;     ...
;   for (int r = 0; r < 16; ++r) p0[r] = __builtin_amdgcn_exp2f(p0[r]);
; }
; __device__ __forceinline__ void finishSM(f32x16& p0, f32x16& p1, float alpha, float& l_reg, v8i& pa) {
; #pragma unroll
;   for (int r = 0; r < 16; ++r) p1[r] = __builtin_amdgcn_exp2f(p1[r]);
;   float ps = 0;
; #pragma unroll
;   for (int r = 0; r < 16; ++r) ps += p0[r];
; #pragma unroll
;   for (int r = 0; r < 16; ++r) ps += p1[r];
;   { auto rr = __builtin_amdgcn_permlane32_swap(__float_as_uint(ps), __float_as_uint(ps), false, false);
;     ps = __uint_as_float(rr[0]) + __uint_as_float(rr[1]); }
;   l_reg = l_reg * alpha + ps;
; #pragma unroll
;   for (int q = 0; q < 4; ++q) { int w0 = pa[q], w1 = pa[4 + q];
;     w0 = __builtin_amdgcn_cvt_pk_fp8_f32(p0[4 * q], p0[4 * q + 1], w0, false); w0 = __builtin_amdgcn_cvt_pk_fp8_f32(p0[4 * q + 2], p0[4 * q + 3], w0, true);
;     w1 = __builtin_amdgcn_cvt_pk_fp8_f32(p1[4 * q], p1[4 * q + 1], w1, false); w1 = __builtin_amdgcn_cvt_pk_fp8_f32(p1[4 * q + 2], p1[4 * q + 3], w1, true);
;     pa[q] = w0; pa[4 + q] = w1; }
; }
; __device__ __forceinline__ void qkt(f32x16& p0, f32x16& p1, const char* Ks, const v8i* qr, int r32, int hi, const f32x16& nm16) {
; #pragma unroll
;   for (int s = 0; s < 3; ++s) { const int c0 = 4 * s + 2 * hi;
;     const v8i a0 = __builtin_shufflevector(*reinterpret_cast<const v4i*>(Ks + k8_off(r32, c0)), *reinterpret_cast<const v4i*>(Ks + k8_off(r32, c0 + 1)), 0, 1, 2, 3, 4, 5, 6, 7);
;     const v8i a1 = __builtin_shufflevector(*reinterpret_cast<const v4i*>(Ks + 32 * DQK + k8_off(r32, c0)), *reinterpret_cast<const v4i*>(Ks + 32 * DQK + k8_off(r32, c0 + 1)), 0, 1, 2, 3, 4, 5, 6, 7);
;     p0 = __builtin_amdgcn_mfma_scale_f32_32x32x64_f8f6f4(a0, qr[s], s == 0 ? nm16 : p0, 0, 0, 0, 0, 0, 0);
;     p1 = __builtin_amdgcn_mfma_scale_f32_32x32x64_f8f6f4(a1, qr[s], s == 0 ? nm16 : p1, 0, 0, 0, 0, 0, 0); }
; }
.Lstg_end3_l0:
	v_exp_f32_e32 v182, v114
	v_exp_f32_e32 v183, v115
	v_exp_f32_e32 v184, v116
	v_exp_f32_e32 v185, v117
	v_exp_f32_e32 v234, v118
	v_exp_f32_e32 v235, v119
	v_exp_f32_e32 v236, v120
	v_exp_f32_e32 v237, v121
	v_exp_f32_e32 v238, v122
	v_exp_f32_e32 v239, v123
	v_exp_f32_e32 v240, v124
	v_exp_f32_e32 v241, v125
	v_exp_f32_e32 v242, v126
	v_exp_f32_e32 v243, v127
	v_exp_f32_e32 v244, v128
	v_exp_f32_e32 v245, v129
	ds_read_b128 v[98:101], v196 offset:49152
	ds_read_b128 v[102:105], v197 offset:49152
	ds_read_b128 v[218:221], v196 offset:55296
	ds_read_b128 v[222:225], v197 offset:55296
	v_exp_f32_e32 v82, v82
	v_exp_f32_e32 v83, v83
	s_waitcnt lgkmcnt(0)
	v_mfma_f32_32x32x64_f8f6f4 v[114:129], v[98:105], v[138:145], v[66:81]
	v_exp_f32_e32 v84, v84
	v_exp_f32_e32 v85, v85
	v_exp_f32_e32 v86, v86
	v_exp_f32_e32 v87, v87
	v_exp_f32_e32 v88, v88
	v_exp_f32_e32 v89, v89
	v_exp_f32_e32 v90, v90
	v_exp_f32_e32 v91, v91
	v_exp_f32_e32 v92, v92
	v_exp_f32_e32 v94, v94
	v_exp_f32_e32 v95, v95
	v_exp_f32_e32 v93, v93
	v_exp_f32_e32 v96, v96
	v_exp_f32_e32 v97, v97
	v_cvt_pk_fp8_f32 v130, v182, v183
	v_mfma_f32_32x32x64_f8f6f4 v[98:113], v[218:225], v[138:145], v[66:81]
	ds_read_b128 v[218:221], v198 offset:49152
	ds_read_b128 v[222:225], v199 offset:49152
	ds_read_b128 v[226:229], v198 offset:55296
	ds_read_b128 v[230:233], v199 offset:55296
	v_cvt_pk_fp8_f32 v134, v82, v83
	v_cvt_pk_fp8_f32 v131, v234, v235
	v_cvt_pk_fp8_f32 v135, v86, v87
	v_cvt_pk_fp8_f32 v132, v238, v239
	v_cvt_pk_fp8_f32 v136, v90, v91
	v_cvt_pk_fp8_f32 v133, v242, v243
	v_cvt_pk_fp8_f32 v137, v94, v95
	v_cvt_pk_fp8_f32 v130, v184, v185 op_sel:[0,0,1]
	v_cvt_pk_fp8_f32 v134, v84, v85 op_sel:[0,0,1]
	v_cvt_pk_fp8_f32 v131, v236, v237 op_sel:[0,0,1]
	v_cvt_pk_fp8_f32 v135, v88, v89 op_sel:[0,0,1]
	v_cvt_pk_fp8_f32 v132, v240, v241 op_sel:[0,0,1]
	v_cvt_pk_fp8_f32 v136, v92, v93 op_sel:[0,0,1]
	v_cvt_pk_fp8_f32 v133, v244, v245 op_sel:[0,0,1]
	s_waitcnt lgkmcnt(0)
	v_mfma_f32_32x32x64_f8f6f4 v[114:129], v[218:225], v[146:153], v[114:129]
	v_cvt_pk_fp8_f32 v137, v96, v97 op_sel:[0,0,1]
	v_mfma_f32_32x32x64_f8f6f4 v[98:113], v[226:233], v[146:153], v[98:113]
	ds_read_b128 v[218:221], v200 offset:49152
	ds_read_b128 v[222:225], v201 offset:49152
	ds_read_b128 v[226:229], v200 offset:55296
	ds_read_b128 v[230:233], v201 offset:55296
	s_setprio 1
	s_waitcnt lgkmcnt(0)
	v_mfma_f32_32x32x64_f8f6f4 v[114:129], v[218:225], v[154:161], v[114:129]
	v_add_f32_e32 v218, 0, v182
	v_add_f32_e32 v218, v183, v218
	v_add_f32_e32 v218, v184, v218
	v_add_f32_e32 v218, v185, v218
	v_add_f32_e32 v218, v234, v218
	v_add_f32_e32 v218, v235, v218
	v_add_f32_e32 v218, v236, v218
	v_add_f32_e32 v218, v237, v218
	v_add_f32_e32 v218, v238, v218
	v_add_f32_e32 v218, v239, v218
	v_add_f32_e32 v218, v240, v218
	v_add_f32_e32 v218, v241, v218
	v_add_f32_e32 v218, v242, v218
	v_add_f32_e32 v218, v243, v218
	v_add_f32_e32 v218, v244, v218
	v_add_f32_e32 v218, v245, v218
	v_add_f32_e32 v218, v82, v218
	v_add_f32_e32 v218, v83, v218
	v_mfma_f32_32x32x64_f8f6f4 v[98:113], v[226:233], v[154:161], v[98:113]
	v_add_f32_e32 v218, v84, v218
	v_add_f32_e32 v218, v85, v218
	v_add_f32_e32 v218, v86, v218
	v_add_f32_e32 v218, v87, v218
	v_add_f32_e32 v218, v88, v218
	v_add_f32_e32 v218, v89, v218
	v_add_f32_e32 v218, v90, v218
	v_add_f32_e32 v218, v91, v218
	v_add_f32_e32 v218, v92, v218
	v_add_f32_e32 v218, v93, v218
	v_add_f32_e32 v218, v94, v218
	v_add_f32_e32 v218, v95, v218
	v_add_f32_e32 v218, v96, v218
	v_add_f32_e32 v218, v97, v218
	v_mov_b32_e32 v219, v218
	s_nop 1
	v_permlane32_swap_b32_e32 v218, v219
	s_cmp_eq_u32 s94, 0
	s_cbranch_scc0 .Lstg_mid4_l0
	s_waitcnt vmcnt(0)
	s_barrier
	s_mov_b32 m0, s92
	s_nop 0
	global_load_lds_dwordx4 v164, s[24:25]
	s_mov_b32 m0, s86
	s_nop 0
	global_load_lds_dwordx4 v170, s[26:27]
	s_add_u32 s24, s24, 0x3000
	s_addc_u32 s25, s25, 0
	s_add_u32 s26, s26, 64
	s_addc_u32 s27, s27, 0

; __device__ __forceinline__ void finishSM(f32x16& p0, f32x16& p1, float alpha, float& l_reg, v8i& pa) {
; #pragma unroll
;   for (int r = 0; r < 16; ++r) p1[r] = __builtin_amdgcn_exp2f(p1[r]);
;   float ps = 0;
; #pragma unroll
;   for (int r = 0; r < 16; ++r) ps += p0[r];
; #pragma unroll
;   for (int r = 0; r < 16; ++r) ps += p1[r];
;   { auto rr = __builtin_amdgcn_permlane32_swap(__float_as_uint(ps), __float_as_uint(ps), false, false);
;     ps = __uint_as_float(rr[0]) + __uint_as_float(rr[1]); }
;   l_reg = l_reg * alpha + ps;
; #pragma unroll
;   for (int q = 0; q < 4; ++q) { int w0 = pa[q], w1 = pa[4 + q];
;     w0 = __builtin_amdgcn_cvt_pk_fp8_f32(p0[4 * q], p0[4 * q + 1], w0, false); w0 = __builtin_amdgcn_cvt_pk_fp8_f32(p0[4 * q + 2], p0[4 * q + 3], w0, true);
;     w1 = __builtin_amdgcn_cvt_pk_fp8_f32(p1[4 * q], p1[4 * q + 1], w1, false); w1 = __builtin_amdgcn_cvt_pk_fp8_f32(p1[4 * q + 2], p1[4 * q + 3], w1, true);
;     pa[q] = w0; pa[4 + q] = w1; }
; }
; __device__ __forceinline__ void qkt(f32x16& p0, f32x16& p1, const char* Ks, const v8i* qr, int r32, int hi, const f32x16& nm16) {
; #pragma unroll
;   for (int s = 0; s < 3; ++s) { const int c0 = 4 * s + 2 * hi;
;     const v8i a0 = __builtin_shufflevector(*reinterpret_cast<const v4i*>(Ks + k8_off(r32, c0)), *reinterpret_cast<const v4i*>(Ks + k8_off(r32, c0 + 1)), 0, 1, 2, 3, 4, 5, 6, 7);
;     const v8i a1 = __builtin_shufflevector(*reinterpret_cast<const v4i*>(Ks + 32 * DQK + k8_off(r32, c0)), *reinterpret_cast<const v4i*>(Ks + 32 * DQK + k8_off(r32, c0 + 1)), 0, 1, 2, 3, 4, 5, 6, 7);
;     p0 = __builtin_amdgcn_mfma_scale_f32_32x32x64_f8f6f4(a0, qr[s], s == 0 ? nm16 : p0, 0, 0, 0, 0, 0, 0);
;     p1 = __builtin_amdgcn_mfma_scale_f32_32x32x64_f8f6f4(a1, qr[s], s == 0 ? nm16 : p1, 0, 0, 0, 0, 0, 0); }
; }
.Lstg_end4_l0:
	v_exp_f32_e32 v176, v114
	v_exp_f32_e32 v177, v115
	v_exp_f32_e32 v178, v116
	v_exp_f32_e32 v179, v117
	v_exp_f32_e32 v180, v118
	v_exp_f32_e32 v181, v119
	v_exp_f32_e32 v182, v120
	v_exp_f32_e32 v183, v121
	v_exp_f32_e32 v184, v122
	v_exp_f32_e32 v185, v123
	v_exp_f32_e32 v221, v124
	v_exp_f32_e32 v238, v125
	v_exp_f32_e32 v239, v126
	v_exp_f32_e32 v240, v127
	v_exp_f32_e32 v241, v128
	v_exp_f32_e32 v242, v129
	ds_read_b128 v[82:85], v196 offset:8192
	ds_read_b128 v[86:89], v197 offset:8192
	ds_read_b128 v[222:225], v196 offset:14336
	ds_read_b128 v[226:229], v197 offset:14336
	v_exp_f32_e32 v100, v100
	v_exp_f32_e32 v101, v101
	s_waitcnt lgkmcnt(0)
	v_mfma_f32_32x32x64_f8f6f4 v[114:129], v[82:89], v[138:145], v[66:81]
	v_exp_f32_e32 v102, v102
	v_exp_f32_e32 v103, v103
	v_exp_f32_e32 v104, v104
	v_exp_f32_e32 v105, v105
	v_exp_f32_e32 v106, v106
	v_exp_f32_e32 v107, v107
	v_exp_f32_e32 v108, v108
	v_exp_f32_e32 v110, v110
	v_exp_f32_e32 v111, v111
	v_exp_f32_e32 v109, v109
	v_exp_f32_e32 v112, v112
	v_exp_f32_e32 v113, v113
	v_cvt_pk_fp8_f32 v130, v176, v177
	v_cvt_pk_fp8_f32 v131, v180, v181
	v_cvt_pk_fp8_f32 v135, v102, v103
	v_mfma_f32_32x32x64_f8f6f4 v[82:97], v[222:229], v[138:145], v[66:81]
	ds_read_b128 v[222:225], v198 offset:8192
	ds_read_b128 v[226:229], v199 offset:8192
	ds_read_b128 v[230:233], v198 offset:14336
	ds_read_b128 v[234:237], v199 offset:14336
	v_cvt_pk_fp8_f32 v132, v184, v185
	v_cvt_pk_fp8_f32 v136, v106, v107
	v_cvt_pk_fp8_f32 v133, v239, v240
	v_cvt_pk_fp8_f32 v137, v110, v111
	v_cvt_pk_fp8_f32 v130, v178, v179 op_sel:[0,0,1]
	v_cvt_pk_fp8_f32 v131, v182, v183 op_sel:[0,0,1]
	v_cvt_pk_fp8_f32 v135, v104, v105 op_sel:[0,0,1]
	v_cvt_pk_fp8_f32 v132, v221, v238 op_sel:[0,0,1]
	v_cvt_pk_fp8_f32 v136, v108, v109 op_sel:[0,0,1]
	v_cvt_pk_fp8_f32 v133, v241, v242 op_sel:[0,0,1]
	v_cvt_pk_fp8_f32 v137, v112, v113 op_sel:[0,0,1]
	s_waitcnt lgkmcnt(0)
	v_mfma_f32_32x32x64_f8f6f4 v[114:129], v[222:229], v[146:153], v[114:129]
	v_mfma_f32_32x32x64_f8f6f4 v[82:97], v[230:237], v[146:153], v[82:97]
	ds_read_b128 v[222:225], v200 offset:8192
	ds_read_b128 v[226:229], v201 offset:8192
	ds_read_b128 v[230:233], v200 offset:14336
	ds_read_b128 v[234:237], v201 offset:14336
	s_setprio 1
	s_waitcnt lgkmcnt(0)
	v_mfma_f32_32x32x64_f8f6f4 v[114:129], v[222:229], v[154:161], v[114:129]
	v_exp_f32_e32 v222, v98
	v_add_f32_e32 v98, 0, v176
	v_add_f32_e32 v98, v177, v98
	v_add_f32_e32 v98, v178, v98
	v_add_f32_e32 v98, v179, v98
	v_add_f32_e32 v98, v180, v98
	v_add_f32_e32 v98, v181, v98
	v_add_f32_e32 v98, v182, v98
	v_add_f32_e32 v98, v183, v98
	v_add_f32_e32 v98, v184, v98
	v_add_f32_e32 v98, v185, v98
	v_add_f32_e32 v98, v221, v98
	v_add_f32_e32 v98, v238, v98
	v_add_f32_e32 v98, v239, v98
	v_exp_f32_e32 v223, v99
	v_add_f32_e32 v98, v240, v98
	v_add_f32_e32 v98, v241, v98
	v_add_f32_e32 v98, v242, v98
	v_add_f32_e32 v98, v222, v98
	v_add_f32_e32 v98, v223, v98
	v_mfma_f32_32x32x64_f8f6f4 v[82:97], v[230:237], v[154:161], v[82:97]
	v_add_f32_e32 v98, v100, v98
	v_add_f32_e32 v98, v101, v98
	v_add_f32_e32 v98, v102, v98
	v_add_f32_e32 v98, v103, v98
	v_add_f32_e32 v98, v104, v98
	v_add_f32_e32 v98, v105, v98
	v_add_f32_e32 v98, v106, v98
	v_add_f32_e32 v98, v107, v98
	v_add_f32_e32 v98, v108, v98
	v_cvt_pk_fp8_f32 v134, v222, v223
	v_add_f32_e32 v98, v109, v98
	v_add_f32_e32 v98, v110, v98
	v_add_f32_e32 v98, v111, v98
	v_add_f32_e32 v98, v112, v98
	v_cvt_pk_fp8_f32 v134, v100, v101 op_sel:[0,0,1]
	v_add_f32_e32 v98, v113, v98
	v_mov_b32_e32 v99, v98
	s_nop 1
	v_permlane32_swap_b32_e32 v98, v99
	s_cmp_eq_u32 s94, 0
	s_cbranch_scc0 .Lstg_mid5_l0
	s_waitcnt vmcnt(0)
	s_barrier
	s_cmp_lt_i32 s9, 49
	s_cbranch_scc0 .Lstg_mid5_l0
	s_mov_b32 m0, s90
	s_nop 0
	global_load_lds_dwordx4 v164, s[24:25]
	s_mov_b32 m0, s88
	s_nop 0
	global_load_lds_dwordx4 v170, s[26:27]
	s_add_u32 s24, s24, 0x3000
	s_addc_u32 s25, s25, 0
	s_add_u32 s26, s26, 64
	s_addc_u32 s27, s27, 0

; __device__ __forceinline__ void finishSM(f32x16& p0, f32x16& p1, float alpha, float& l_reg, v8i& pa) {
; #pragma unroll
;   for (int r = 0; r < 16; ++r) p1[r] = __builtin_amdgcn_exp2f(p1[r]);
;   float ps = 0;
; #pragma unroll
;   for (int r = 0; r < 16; ++r) ps += p0[r];
; #pragma unroll
;   for (int r = 0; r < 16; ++r) ps += p1[r];
;   { auto rr = __builtin_amdgcn_permlane32_swap(__float_as_uint(ps), __float_as_uint(ps), false, false);
;     ps = __uint_as_float(rr[0]) + __uint_as_float(rr[1]); }
;   l_reg = l_reg * alpha + ps;
; #pragma unroll
;   for (int q = 0; q < 4; ++q) { int w0 = pa[q], w1 = pa[4 + q];
;     w0 = __builtin_amdgcn_cvt_pk_fp8_f32(p0[4 * q], p0[4 * q + 1], w0, false); w0 = __builtin_amdgcn_cvt_pk_fp8_f32(p0[4 * q + 2], p0[4 * q + 3], w0, true);
;     w1 = __builtin_amdgcn_cvt_pk_fp8_f32(p1[4 * q], p1[4 * q + 1], w1, false); w1 = __builtin_amdgcn_cvt_pk_fp8_f32(p1[4 * q + 2], p1[4 * q + 3], w1, true);
;     pa[q] = w0; pa[4 + q] = w1; }
; }
; __device__ __forceinline__ void qkt(f32x16& p0, f32x16& p1, const char* Ks, const v8i* qr, int r32, int hi, const f32x16& nm16) {
; #pragma unroll
;   for (int s = 0; s < 3; ++s) { const int c0 = 4 * s + 2 * hi;
;     const v8i a0 = __builtin_shufflevector(*reinterpret_cast<const v4i*>(Ks + k8_off(r32, c0)), *reinterpret_cast<const v4i*>(Ks + k8_off(r32, c0 + 1)), 0, 1, 2, 3, 4, 5, 6, 7);
;     const v8i a1 = __builtin_shufflevector(*reinterpret_cast<const v4i*>(Ks + 32 * DQK + k8_off(r32, c0)), *reinterpret_cast<const v4i*>(Ks + 32 * DQK + k8_off(r32, c0 + 1)), 0, 1, 2, 3, 4, 5, 6, 7);
;     p0 = __builtin_amdgcn_mfma_scale_f32_32x32x64_f8f6f4(a0, qr[s], s == 0 ? nm16 : p0, 0, 0, 0, 0, 0, 0);
;     p1 = __builtin_amdgcn_mfma_scale_f32_32x32x64_f8f6f4(a1, qr[s], s == 0 ? nm16 : p1, 0, 0, 0, 0, 0, 0); }
; }
.Lstg_end4_l1:
	v_exp_f32_e32 v176, v114
	v_exp_f32_e32 v177, v115
	v_exp_f32_e32 v178, v116
	v_exp_f32_e32 v179, v117
	v_exp_f32_e32 v180, v118
	v_exp_f32_e32 v181, v119
	v_exp_f32_e32 v182, v120
	v_exp_f32_e32 v183, v121
	v_exp_f32_e32 v184, v122
	v_exp_f32_e32 v185, v123
	v_exp_f32_e32 v221, v124
	v_exp_f32_e32 v238, v125
	v_exp_f32_e32 v239, v126
	v_exp_f32_e32 v240, v127
	v_exp_f32_e32 v241, v128
	v_exp_f32_e32 v242, v129
	ds_read_b128 v[82:85], v196 offset:8192
	ds_read_b128 v[86:89], v197 offset:8192
	ds_read_b128 v[222:225], v196 offset:14336
	ds_read_b128 v[226:229], v197 offset:14336
	v_exp_f32_e32 v100, v100
	v_exp_f32_e32 v101, v101
	s_waitcnt lgkmcnt(0)
	v_mfma_f32_32x32x64_f8f6f4 v[114:129], v[82:89], v[138:145], v[66:81]
	v_exp_f32_e32 v102, v102
	v_exp_f32_e32 v103, v103
	v_exp_f32_e32 v104, v104
	v_exp_f32_e32 v105, v105
	v_exp_f32_e32 v106, v106
	v_exp_f32_e32 v107, v107
	v_exp_f32_e32 v108, v108
	v_exp_f32_e32 v110, v110
	v_exp_f32_e32 v111, v111
	v_exp_f32_e32 v109, v109
	v_exp_f32_e32 v112, v112
	v_exp_f32_e32 v113, v113
	v_cvt_pk_fp8_f32 v130, v176, v177
	v_cvt_pk_fp8_f32 v131, v180, v181
	v_cvt_pk_fp8_f32 v135, v102, v103
	v_mfma_f32_32x32x64_f8f6f4 v[82:97], v[222:229], v[138:145], v[66:81]
	ds_read_b128 v[222:225], v198 offset:8192
	ds_read_b128 v[226:229], v199 offset:8192
	ds_read_b128 v[230:233], v198 offset:14336
	ds_read_b128 v[234:237], v199 offset:14336
	v_cvt_pk_fp8_f32 v132, v184, v185
	v_cvt_pk_fp8_f32 v136, v106, v107
	v_cvt_pk_fp8_f32 v133, v239, v240
	v_cvt_pk_fp8_f32 v137, v110, v111
	v_cvt_pk_fp8_f32 v130, v178, v179 op_sel:[0,0,1]
	v_cvt_pk_fp8_f32 v131, v182, v183 op_sel:[0,0,1]
	v_cvt_pk_fp8_f32 v135, v104, v105 op_sel:[0,0,1]
	v_cvt_pk_fp8_f32 v132, v221, v238 op_sel:[0,0,1]
	v_cvt_pk_fp8_f32 v136, v108, v109 op_sel:[0,0,1]
	v_cvt_pk_fp8_f32 v133, v241, v242 op_sel:[0,0,1]
	v_cvt_pk_fp8_f32 v137, v112, v113 op_sel:[0,0,1]
	s_waitcnt lgkmcnt(0)
	v_mfma_f32_32x32x64_f8f6f4 v[114:129], v[222:229], v[146:153], v[114:129]
	v_mfma_f32_32x32x64_f8f6f4 v[82:97], v[230:237], v[146:153], v[82:97]
	ds_read_b128 v[222:225], v200 offset:8192
	ds_read_b128 v[226:229], v201 offset:8192
	ds_read_b128 v[230:233], v200 offset:14336
	ds_read_b128 v[234:237], v201 offset:14336
	s_setprio 1
	s_waitcnt lgkmcnt(0)
	v_mfma_f32_32x32x64_f8f6f4 v[114:129], v[222:229], v[154:161], v[114:129]
	v_exp_f32_e32 v222, v98
	v_add_f32_e32 v98, 0, v176
	v_add_f32_e32 v98, v177, v98
	v_add_f32_e32 v98, v178, v98
	v_add_f32_e32 v98, v179, v98
	v_add_f32_e32 v98, v180, v98
	v_add_f32_e32 v98, v181, v98
	v_add_f32_e32 v98, v182, v98
	v_add_f32_e32 v98, v183, v98
	v_add_f32_e32 v98, v184, v98
	v_add_f32_e32 v98, v185, v98
	v_add_f32_e32 v98, v221, v98
	v_add_f32_e32 v98, v238, v98
	v_add_f32_e32 v98, v239, v98
	v_exp_f32_e32 v223, v99
	v_add_f32_e32 v98, v240, v98
	v_add_f32_e32 v98, v241, v98
	v_add_f32_e32 v98, v242, v98
	v_add_f32_e32 v98, v222, v98
	v_add_f32_e32 v98, v223, v98
	v_mfma_f32_32x32x64_f8f6f4 v[82:97], v[230:237], v[154:161], v[82:97]
	v_add_f32_e32 v98, v100, v98
	v_add_f32_e32 v98, v101, v98
	v_add_f32_e32 v98, v102, v98
	v_add_f32_e32 v98, v103, v98
	v_add_f32_e32 v98, v104, v98
	v_add_f32_e32 v98, v105, v98
	v_add_f32_e32 v98, v106, v98
	v_add_f32_e32 v98, v107, v98
	v_add_f32_e32 v98, v108, v98
	v_cvt_pk_fp8_f32 v134, v222, v223
	v_add_f32_e32 v98, v109, v98
	v_add_f32_e32 v98, v110, v98
	v_add_f32_e32 v98, v111, v98
	v_add_f32_e32 v98, v112, v98
	v_cvt_pk_fp8_f32 v134, v100, v101 op_sel:[0,0,1]
	v_add_f32_e32 v98, v113, v98
	v_mov_b32_e32 v99, v98
	s_nop 1
	v_permlane32_swap_b32_e32 v98, v99
	s_cmp_eq_u32 s94, 0
	s_cbranch_scc0 .Lstg_mid5_l1
	s_waitcnt vmcnt(0)
	s_barrier
	s_cmp_lt_i32 s8, 49
	s_cbranch_scc0 .Lstg_mid5_l1
	s_mov_b32 m0, s90
	s_nop 0
	global_load_lds_dwordx4 v164, s[24:25]
	s_mov_b32 m0, s88
	s_nop 0
	global_load_lds_dwordx4 v170, s[26:27]
	s_add_u32 s24, s24, 0x3000
	s_addc_u32 s25, s25, 0
	s_add_u32 s26, s26, 64
	s_addc_u32 s27, s27, 0
